# differential attention: s_setprio 1..0 brackets around each MFMA burst (PV pending, QK, PV)
# speedup vs baseline: 1.0077x; 1.0077x over previous
; #define SBAR() __builtin_amdgcn_sched_barrier(0)
; #define ATT_RDK(X, KS) do { X##0 = tr_read<v_rd_off(0, KS, 0)>(vb); X##1 = tr_read<v_rd_off(0, KS, 1)>(vb); X##2 = tr_read<v_rd_off(1, KS, 0)>(vb); X##3 = tr_read<v_rd_off(1, KS, 1)>(vb); \
;     X##4 = tr_read<v_rd_off(2, KS, 0)>(vb); X##5 = tr_read<v_rd_off(2, KS, 1)>(vb); X##6 = tr_read<v_rd_off(3, KS, 0)>(vb); X##7 = tr_read<v_rd_off(3, KS, 1)>(vb); } while (0)
; #define ATT_MMAK(PA, X) do { o[0] = __builtin_amdgcn_mfma_f32_32x32x16_bf16(PA, ATT_PKV(X##0, X##1), o[0], 0, 0, 0); o[1] = __builtin_amdgcn_mfma_f32_32x32x16_bf16(PA, ATT_PKV(X##2, X##3), o[1], 0, 0, 0); \
;     o[2] = __builtin_amdgcn_mfma_f32_32x32x16_bf16(PA, ATT_PKV(X##4, X##5), o[2], 0, 0, 0); o[3] = __builtin_amdgcn_mfma_f32_32x32x16_bf16(PA, ATT_PKV(X##6, X##7), o[3], 0, 0, 0); } while (0)
; __device__ __forceinline__ void pv_pipe(f32x16* o, int vb, bf16x8 pa0, bf16x8 pa1, bf16x8 pa2, bf16x8 pa3) {
;     s16x4 a0, a1, a2, a3, a4, a5, a6, a7, b0, b1, b2, b3, b4, b5, b6, b7;
;     SBAR(); ATT_RDK(a, 0); ATT_RDK(b, 1);
;     asm volatile("s_waitcnt lgkmcnt(8)" ::: "memory"); SBAR(); ATT_MMAK(pa0, a);
;     SBAR(); ATT_RDK(a, 2);
;     asm volatile("s_waitcnt lgkmcnt(8)" ::: "memory"); SBAR(); ATT_MMAK(pa1, b);
;     SBAR(); ATT_RDK(b, 3);
;     asm volatile("s_waitcnt lgkmcnt(8)" ::: "memory"); SBAR(); ATT_MMAK(pa2, a);
;     asm volatile("s_waitcnt lgkmcnt(0)" ::: "memory"); SBAR(); ATT_MMAK(pa3, b);
; }
; __device__ __forceinline__ void da_unit(LAS unsigned char* lds, const bf16* __restrict__ Q, const bf16* __restrict__ Kp, const bf16* __restrict__ Vp, const float* __restrict__ gda, float lam, ...
;     ...
;         if (comp == 1 && pend) { pv_pipe(o, vb0 + pbuf * SHM_T, pa0, pa1, pa2, pa3); pend = false; }
.LBB0_572:
	v_lshl_add_u32 v99, s29, 14, v169
	ds_read_b64_tr_b16 v[100:101], v99 offset:0
	ds_read_b64_tr_b16 v[102:103], v99 offset:0x800
	ds_read_b64_tr_b16 v[104:105], v99 offset:0x200
	ds_read_b64_tr_b16 v[106:107], v99 offset:0xa00
	ds_read_b64_tr_b16 v[108:109], v99 offset:0x400
	ds_read_b64_tr_b16 v[110:111], v99 offset:0xc00
	ds_read_b64_tr_b16 v[184:185], v99 offset:0x600
	ds_read_b64_tr_b16 v[186:187], v99 offset:0xe00
	ds_read_b64_tr_b16 v[188:189], v99 offset:0x1000
	ds_read_b64_tr_b16 v[190:191], v99 offset:0x1800
	ds_read_b64_tr_b16 v[196:197], v99 offset:0x1200
	ds_read_b64_tr_b16 v[198:199], v99 offset:0x1a00
	ds_read_b64_tr_b16 v[200:201], v99 offset:0x1400
	ds_read_b64_tr_b16 v[202:203], v99 offset:0x1c00
	ds_read_b64_tr_b16 v[204:205], v99 offset:0x1600
	ds_read_b64_tr_b16 v[206:207], v99 offset:0x1e00
	s_waitcnt lgkmcnt(8)
	s_nop 0
	s_setprio 1
	v_mfma_f32_32x32x16_bf16 v[2:17], v[86:89], v[100:103], v[2:17]
	v_mfma_f32_32x32x16_bf16 v[18:33], v[86:89], v[104:107], v[18:33]
	v_mfma_f32_32x32x16_bf16 v[34:49], v[86:89], v[108:111], v[34:49]
	v_mfma_f32_32x32x16_bf16 v[50:65], v[86:89], v[184:187], v[50:65]
	ds_read_b64_tr_b16 v[100:101], v99 offset:0x2000
	ds_read_b64_tr_b16 v[102:103], v99 offset:0x2800
	ds_read_b64_tr_b16 v[104:105], v99 offset:0x2200
	ds_read_b64_tr_b16 v[106:107], v99 offset:0x2a00
	ds_read_b64_tr_b16 v[108:109], v99 offset:0x2400
	ds_read_b64_tr_b16 v[110:111], v99 offset:0x2c00
	ds_read_b64_tr_b16 v[184:185], v99 offset:0x2600
	ds_read_b64_tr_b16 v[186:187], v99 offset:0x2e00
	s_waitcnt lgkmcnt(8)
	v_mfma_f32_32x32x16_bf16 v[2:17], v[94:97], v[188:191], v[2:17]
	v_mfma_f32_32x32x16_bf16 v[18:33], v[94:97], v[196:199], v[18:33]
	v_mfma_f32_32x32x16_bf16 v[34:49], v[94:97], v[200:203], v[34:49]
	v_mfma_f32_32x32x16_bf16 v[50:65], v[94:97], v[204:207], v[50:65]
	ds_read_b64_tr_b16 v[188:189], v99 offset:0x3000
	ds_read_b64_tr_b16 v[190:191], v99 offset:0x3800
	ds_read_b64_tr_b16 v[196:197], v99 offset:0x3200
	ds_read_b64_tr_b16 v[198:199], v99 offset:0x3a00
	ds_read_b64_tr_b16 v[200:201], v99 offset:0x3400
	ds_read_b64_tr_b16 v[202:203], v99 offset:0x3c00
	ds_read_b64_tr_b16 v[204:205], v99 offset:0x3600
	ds_read_b64_tr_b16 v[206:207], v99 offset:0x3e00
	s_waitcnt lgkmcnt(8)
	v_mfma_f32_32x32x16_bf16 v[2:17], v[90:93], v[100:103], v[2:17]
	s_waitcnt lgkmcnt(0)
	v_mfma_f32_32x32x16_bf16 v[18:33], v[90:93], v[104:107], v[18:33]
	v_mfma_f32_32x32x16_bf16 v[34:49], v[90:93], v[108:111], v[34:49]
	v_mfma_f32_32x32x16_bf16 v[50:65], v[90:93], v[184:187], v[50:65]
	v_mfma_f32_32x32x16_bf16 v[2:17], v[82:85], v[188:191], v[2:17]
	v_mfma_f32_32x32x16_bf16 v[18:33], v[82:85], v[196:199], v[18:33]
	v_mfma_f32_32x32x16_bf16 v[34:49], v[82:85], v[200:203], v[34:49]
	v_mfma_f32_32x32x16_bf16 v[50:65], v[82:85], v[204:207], v[50:65]
	s_setprio 0

; #define SBAR() __builtin_amdgcn_sched_barrier(0)
; #define ATT_RDK(X, KS) do { X##0 = tr_read<v_rd_off(0, KS, 0)>(vb); X##1 = tr_read<v_rd_off(0, KS, 1)>(vb); X##2 = tr_read<v_rd_off(1, KS, 0)>(vb); X##3 = tr_read<v_rd_off(1, KS, 1)>(vb); \
;     X##4 = tr_read<v_rd_off(2, KS, 0)>(vb); X##5 = tr_read<v_rd_off(2, KS, 1)>(vb); X##6 = tr_read<v_rd_off(3, KS, 0)>(vb); X##7 = tr_read<v_rd_off(3, KS, 1)>(vb); } while (0)
; #define ATT_MMAK(PA, X) do { o[0] = __builtin_amdgcn_mfma_f32_32x32x16_bf16(PA, ATT_PKV(X##0, X##1), o[0], 0, 0, 0); o[1] = __builtin_amdgcn_mfma_f32_32x32x16_bf16(PA, ATT_PKV(X##2, X##3), o[1], 0, 0, 0); \
;     o[2] = __builtin_amdgcn_mfma_f32_32x32x16_bf16(PA, ATT_PKV(X##4, X##5), o[2], 0, 0, 0); o[3] = __builtin_amdgcn_mfma_f32_32x32x16_bf16(PA, ATT_PKV(X##6, X##7), o[3], 0, 0, 0); } while (0)
; __device__ __forceinline__ void pv_pipe(f32x16* o, int vb, bf16x8 pa0, bf16x8 pa1, bf16x8 pa2, bf16x8 pa3) {
;     s16x4 a0, a1, a2, a3, a4, a5, a6, a7, b0, b1, b2, b3, b4, b5, b6, b7;
;     SBAR(); ATT_RDK(a, 0); ATT_RDK(b, 1);
;     asm volatile("s_waitcnt lgkmcnt(8)" ::: "memory"); SBAR(); ATT_MMAK(pa0, a);
;     SBAR(); ATT_RDK(a, 2);
;     asm volatile("s_waitcnt lgkmcnt(8)" ::: "memory"); SBAR(); ATT_MMAK(pa1, b);
;     SBAR(); ATT_RDK(b, 3);
;     asm volatile("s_waitcnt lgkmcnt(8)" ::: "memory"); SBAR(); ATT_MMAK(pa2, a);
;     asm volatile("s_waitcnt lgkmcnt(0)" ::: "memory"); SBAR(); ATT_MMAK(pa3, b);
; }
; __device__ __forceinline__ void da_unit(LAS unsigned char* lds, const bf16* __restrict__ Q, const bf16* __restrict__ Kp, const bf16* __restrict__ Vp, const float* __restrict__ gda, float lam, ...
;     ...
;             if (comp == 0) pv_pipe(o, vb0 + vbuf * SHM_T, pa0, pa1, pa2, pa3); else { pend = true; pbuf = vbuf; }
.LBB0_583:
	v_lshl_add_u32 v195, s25, 14, v169
	ds_read_b64_tr_b16 v[98:99], v195 offset:0
	ds_read_b64_tr_b16 v[100:101], v195 offset:0x800
	ds_read_b64_tr_b16 v[102:103], v195 offset:0x200
	ds_read_b64_tr_b16 v[104:105], v195 offset:0xa00
	ds_read_b64_tr_b16 v[106:107], v195 offset:0x400
	ds_read_b64_tr_b16 v[108:109], v195 offset:0xc00
	ds_read_b64_tr_b16 v[110:111], v195 offset:0x600
	ds_read_b64_tr_b16 v[112:113], v195 offset:0xe00
	ds_read_b64_tr_b16 v[182:183], v195 offset:0x1000
	ds_read_b64_tr_b16 v[184:185], v195 offset:0x1800
	ds_read_b64_tr_b16 v[186:187], v195 offset:0x1200
	ds_read_b64_tr_b16 v[188:189], v195 offset:0x1a00
	ds_read_b64_tr_b16 v[190:191], v195 offset:0x1400
	ds_read_b64_tr_b16 v[192:193], v195 offset:0x1c00
	ds_read_b64_tr_b16 v[196:197], v195 offset:0x1600
	ds_read_b64_tr_b16 v[198:199], v195 offset:0x1e00
	s_waitcnt lgkmcnt(8)
	s_nop 0
	s_setprio 1
	v_mfma_f32_32x32x16_bf16 v[2:17], v[86:89], v[98:101], v[2:17]
	v_mfma_f32_32x32x16_bf16 v[18:33], v[86:89], v[102:105], v[18:33]
	v_mfma_f32_32x32x16_bf16 v[34:49], v[86:89], v[106:109], v[34:49]
	v_mfma_f32_32x32x16_bf16 v[50:65], v[86:89], v[110:113], v[50:65]
	ds_read_b64_tr_b16 v[98:99], v195 offset:0x2000
	ds_read_b64_tr_b16 v[100:101], v195 offset:0x2800
	ds_read_b64_tr_b16 v[102:103], v195 offset:0x2200
	ds_read_b64_tr_b16 v[104:105], v195 offset:0x2a00
	ds_read_b64_tr_b16 v[106:107], v195 offset:0x2400
	ds_read_b64_tr_b16 v[108:109], v195 offset:0x2c00
	ds_read_b64_tr_b16 v[110:111], v195 offset:0x2600
	ds_read_b64_tr_b16 v[112:113], v195 offset:0x2e00
	s_waitcnt lgkmcnt(8)
	v_mfma_f32_32x32x16_bf16 v[2:17], v[94:97], v[182:185], v[2:17]
	v_mfma_f32_32x32x16_bf16 v[18:33], v[94:97], v[186:189], v[18:33]
	v_mfma_f32_32x32x16_bf16 v[34:49], v[94:97], v[190:193], v[34:49]
	v_mfma_f32_32x32x16_bf16 v[50:65], v[94:97], v[196:199], v[50:65]
	ds_read_b64_tr_b16 v[182:183], v195 offset:0x3000
	ds_read_b64_tr_b16 v[184:185], v195 offset:0x3800
	ds_read_b64_tr_b16 v[186:187], v195 offset:0x3200
	ds_read_b64_tr_b16 v[188:189], v195 offset:0x3a00
	ds_read_b64_tr_b16 v[190:191], v195 offset:0x3400
	ds_read_b64_tr_b16 v[192:193], v195 offset:0x3c00
	ds_read_b64_tr_b16 v[196:197], v195 offset:0x3600
	ds_read_b64_tr_b16 v[198:199], v195 offset:0x3e00
	s_waitcnt lgkmcnt(8)
	v_mfma_f32_32x32x16_bf16 v[2:17], v[90:93], v[98:101], v[2:17]
	s_waitcnt lgkmcnt(0)
	v_mfma_f32_32x32x16_bf16 v[18:33], v[90:93], v[102:105], v[18:33]
	v_mfma_f32_32x32x16_bf16 v[34:49], v[90:93], v[106:109], v[34:49]
	v_mfma_f32_32x32x16_bf16 v[50:65], v[90:93], v[110:113], v[50:65]
	v_mfma_f32_32x32x16_bf16 v[2:17], v[82:85], v[182:185], v[2:17]
	s_mov_b64 s[18:19], 0
	v_mfma_f32_32x32x16_bf16 v[18:33], v[82:85], v[186:189], v[18:33]
	v_mfma_f32_32x32x16_bf16 v[34:49], v[82:85], v[190:193], v[34:49]
	v_mfma_f32_32x32x16_bf16 v[50:65], v[82:85], v[196:199], v[50:65]
	s_setprio 0
	s_add_i32 s8, s27, 3
	s_cmp_ge_u32 s8, s26
	s_cbranch_scc1 .LBB0_574
; #define LAS __attribute__((address_space(3)))
; #define SBAR() __builtin_amdgcn_sched_barrier(0)
; __device__ __forceinline__ void da_unit(LAS unsigned char* lds, const bf16* __restrict__ Q, const bf16* __restrict__ Kp, const bf16* __restrict__ Vp, const float* __restrict__ gda, float lam, ...
;     ...
;             f32x16 p0 = mneg, p1 = mneg;
;             { const LAS unsigned char* Ks = K_lds + buf * SHM_T; bf16x8 kb0[4], kb1[4];
; #pragma unroll
;               for (int d0 = 0; d0 < 4; ++d0) { const int cb = (comp * 64 + d0 * 16 + hi * 8) * 2;
;                   kb0[d0] = *(const LAS bf16x8*)(Ks + KSWZ(r32, cb)); kb1[d0] = *(const LAS bf16x8*)(Ks + KSWZ(32 + r32, cb)); }
;               SBAR();
; #pragma unroll
;               for (int d0 = 0; d0 < 4; ++d0) { p0 = __builtin_amdgcn_mfma_f32_32x32x16_bf16(kb0[d0], qr[d0], p0, 0, 0, 0); p1 = __builtin_amdgcn_mfma_f32_32x32x16_bf16(kb1[d0], qr[d0], p1, 0, 0, 0); } }
;             if (j == 0) {
; #pragma unroll
;                 for (int r = 0; r < 16; ++r) p0[r] = -INFINITY;
; #pragma unroll
;                 for (int r = 0; r < 8; ++r) p1[r] = -INFINITY;
;             }
;             float pmax = p0[0];
; #pragma unroll
;             for (int r = 1; r < 16; ++r) pmax = fmaxf(pmax, p0[r]);
; #pragma unroll
;             for (int r = 0; r < 16; ++r) pmax = fmaxf(pmax, p1[r]);
;             { auto rr = __builtin_amdgcn_permlane32_swap(__builtin_bit_cast(unsigned, pmax), __builtin_bit_cast(unsigned, pmax), false, false);
;               pmax = fmaxf(__builtin_bit_cast(float, rr[0]), __builtin_bit_cast(float, rr[1])); }
;             float alpha = 1.f;
;             if (j == 0 || !__all(pmax <= THR2)) {
;                 const float dl = j == 0 ? pmax : fmaxf(pmax, 0.f);
;                 alpha = j == 0 ? 1.f : __builtin_amdgcn_exp2f(-dl); m_reg += dl;
; #pragma unroll
;                 for (int r = 0; r < 16; ++r) { p0[r] -= dl; p1[r] -= dl; mneg[r] = -m_reg; }
.LBB0_584:
	s_lshl_b32 s8, s23, 14
	s_add_i32 s8, s8, 0
	s_add_i32 s8, s8, 0x10000
	v_add_u32_e32 v82, s8, v165
	v_add_u32_e32 v83, s8, v170
	v_add_u32_e32 v84, v82, v173
	v_add_u32_e32 v85, v83, v173
	ds_read_b128 v[98:101], v84
	ds_read_b128 v[182:185], v85
	v_add_u32_e32 v84, v82, v174
	v_add_u32_e32 v85, v83, v174
	ds_read_b128 v[186:189], v84
	ds_read_b128 v[190:193], v85
	v_add_u32_e32 v84, v82, v175
	v_add_u32_e32 v82, v82, v176
	v_add_u32_e32 v85, v83, v175
	ds_read_b128 v[196:199], v84
	ds_read_b128 v[200:203], v85
	v_add_u32_e32 v83, v83, v176
	ds_read_b128 v[204:207], v82
	ds_read_b128 v[208:211], v83
	s_waitcnt lgkmcnt(7)
	s_setprio 1
	v_mfma_f32_32x32x16_bf16 v[82:97], v[98:101], v[114:117], v[66:81]
	v_mov_b64_e32 v[112:113], v[80:81]
	v_mov_b64_e32 v[110:111], v[78:79]
	v_mov_b64_e32 v[108:109], v[76:77]
	v_mov_b64_e32 v[106:107], v[74:75]
	v_mov_b64_e32 v[104:105], v[72:73]
	v_mov_b64_e32 v[102:103], v[70:71]
	v_mov_b64_e32 v[100:101], v[68:69]
	v_mov_b64_e32 v[98:99], v[66:67]
	s_waitcnt lgkmcnt(5)
	v_mfma_f32_32x32x16_bf16 v[82:97], v[186:189], v[118:121], v[82:97]
	s_mov_b32 s8, 0x4138aa3b
	v_mfma_f32_32x32x16_bf16 v[98:113], v[182:185], v[114:117], v[98:113]
	s_waitcnt lgkmcnt(3)
	v_mfma_f32_32x32x16_bf16 v[82:97], v[196:199], v[122:125], v[82:97]
	v_mfma_f32_32x32x16_bf16 v[98:113], v[190:193], v[118:121], v[98:113]
	s_waitcnt lgkmcnt(1)
	v_mfma_f32_32x32x16_bf16 v[82:97], v[204:207], v[126:129], v[82:97]
	v_mfma_f32_32x32x16_bf16 v[98:113], v[200:203], v[122:125], v[98:113]
	s_nop 10
	v_max_f32_e32 v182, v83, v83
	v_max_f32_e32 v183, v82, v82
	v_max_f32_e32 v182, v183, v182
	v_max3_f32 v182, v182, v84, v85
	v_max3_f32 v182, v182, v86, v87
	v_max3_f32 v182, v182, v88, v89
	v_max3_f32 v182, v182, v90, v91
	s_waitcnt lgkmcnt(0)
	v_mfma_f32_32x32x16_bf16 v[98:113], v[208:211], v[126:129], v[98:113]
	s_setprio 0
	v_max3_f32 v182, v182, v92, v93
	v_max3_f32 v182, v182, v94, v95
	v_max3_f32 v182, v182, v96, v97
	s_nop 8
	v_max3_f32 v182, v182, v98, v99
	v_max3_f32 v182, v182, v100, v101
	v_max3_f32 v182, v182, v102, v103
	v_max3_f32 v182, v182, v104, v105
	v_max3_f32 v182, v182, v106, v107
	v_max3_f32 v182, v182, v108, v109
	v_max3_f32 v182, v182, v110, v111
	v_max3_f32 v183, v182, v112, v113
	v_mov_b32_e32 v182, v183
	s_nop 1
	v_permlane32_swap_b32_e32 v183, v182
	v_cmp_ge_f32_e32 vcc, s8, v183
	s_cmp_eq_u64 vcc, exec
	v_mov_b32_e32 v182, 1.0
	s_cbranch_scc1 .LBB0_586
	v_max_f32_e32 v66, v183, v183
	v_max_f32_e32 v68, 0, v66
	v_exp_f32_e64 v182, -v68
	v_add_f32_e32 v151, v151, v68
	v_xor_b32_e32 v66, 0x80000000, v151
	v_pk_add_f32 v[82:83], v[82:83], v[68:69] op_sel_hi:[1,0] neg_lo:[0,1] neg_hi:[0,1]
	v_pk_add_f32 v[98:99], v[98:99], v[68:69] op_sel_hi:[1,0] neg_lo:[0,1] neg_hi:[0,1]
	v_pk_add_f32 v[84:85], v[84:85], v[68:69] op_sel_hi:[1,0] neg_lo:[0,1] neg_hi:[0,1]
	v_pk_add_f32 v[100:101], v[100:101], v[68:69] op_sel_hi:[1,0] neg_lo:[0,1] neg_hi:[0,1]
	v_pk_add_f32 v[86:87], v[86:87], v[68:69] op_sel_hi:[1,0] neg_lo:[0,1] neg_hi:[0,1]
	v_pk_add_f32 v[102:103], v[102:103], v[68:69] op_sel_hi:[1,0] neg_lo:[0,1] neg_hi:[0,1]
	v_pk_add_f32 v[88:89], v[88:89], v[68:69] op_sel_hi:[1,0] neg_lo:[0,1] neg_hi:[0,1]
	v_pk_add_f32 v[104:105], v[104:105], v[68:69] op_sel_hi:[1,0] neg_lo:[0,1] neg_hi:[0,1]
	v_pk_add_f32 v[90:91], v[90:91], v[68:69] op_sel_hi:[1,0] neg_lo:[0,1] neg_hi:[0,1]
	v_pk_add_f32 v[106:107], v[106:107], v[68:69] op_sel_hi:[1,0] neg_lo:[0,1] neg_hi:[0,1]
	v_pk_add_f32 v[92:93], v[92:93], v[68:69] op_sel_hi:[1,0] neg_lo:[0,1] neg_hi:[0,1]
	v_pk_add_f32 v[108:109], v[108:109], v[68:69] op_sel_hi:[1,0] neg_lo:[0,1] neg_hi:[0,1]
	v_pk_add_f32 v[94:95], v[94:95], v[68:69] op_sel_hi:[1,0] neg_lo:[0,1] neg_hi:[0,1]
	v_pk_add_f32 v[110:111], v[110:111], v[68:69] op_sel_hi:[1,0] neg_lo:[0,1] neg_hi:[0,1]
	v_pk_add_f32 v[96:97], v[96:97], v[68:69] op_sel_hi:[1,0] neg_lo:[0,1] neg_hi:[0,1]
	v_pk_add_f32 v[112:113], v[112:113], v[68:69] op_sel_hi:[1,0] neg_lo:[0,1] neg_hi:[0,1]
	v_mov_b32_e32 v67, v66
	v_mov_b32_e32 v68, v66
	v_mov_b32_e32 v69, v66
	v_mov_b32_e32 v70, v66
	v_mov_b32_e32 v71, v66
	v_mov_b32_e32 v72, v66
	v_mov_b32_e32 v73, v66
	v_mov_b32_e32 v74, v66
	v_mov_b32_e32 v75, v66
	v_mov_b32_e32 v76, v66
	v_mov_b32_e32 v77, v66
	v_mov_b32_e32 v78, v66
	v_mov_b32_e32 v79, v66
	v_mov_b32_e32 v80, v66
	v_mov_b32_e32 v81, v66
